# v50 + fp8 GEMM K-loops (P1/5/6/7/11): B-operand LDS read addresses folded into ds_read offset immediates (lane-offset registers biased by the stage base once per unit), 8 VALU fewer per trip
# baseline (speedup 1.0000x reference)
.LBB0_982:
	s_cmpk_lg_i32 s97, 0x180
	s_cbranch_scc1 .Lp1_fast
	v_add_u32_e32 v129, s31, v128
	v_ashrrev_i32_e32 v131, 3, v129
	v_lshlrev_b32_e32 v130, 4, v128
	v_lshlrev_b32_e32 v136, 1, v131
	v_lshrrev_b32_e32 v137, 2, v131
	v_bitop3_b32 v130, v129, s55, v130 bitop3:0x48
	v_and_b32_e32 v136, 24, v136
	v_and_b32_e32 v137, 4, v137
	v_and_b32_e32 v138, 0x1fffe3, v131
	v_lshl_add_u32 v129, v129, 4, v132
	v_or3_b32 v136, v138, v137, v136
	v_ashrrev_i32_e32 v129, 7, v129
	v_lshl_or_b32 v244, v136, 11, v130
	v_lshlrev_b32_e32 v136, 1, v129
	v_lshrrev_b32_e32 v137, 2, v129
	v_and_b32_e32 v136, 24, v136
	v_and_b32_e32 v137, 4, v137
	v_and_b32_e32 v138, 0x1fffe3, v129
	v_or3_b32 v136, v138, v137, v136
	v_lshl_or_b32 v245, v136, 11, v130
	v_and_b32_e32 v136, 15, v128
	v_lshrrev_b32_e32 v137, 3, v128
	v_bfe_u32 v128, v128, 1, 3
	s_mov_b32 s10, 0xffffffe
	v_lshlrev_b32_e32 v136, 7, v136
	v_and_b32_e32 v138, 0xffffffe, v137
	v_bitop3_b32 v137, v137, v128, s10 bitop3:0x6c
	v_or_b32_e32 v168, s70, v136
	v_or_b32_e32 v136, s71, v136
	v_lshlrev_b32_e32 v169, 4, v137
	v_bitop3_b32 v128, v138, v128, 1 bitop3:0x36
	v_add3_u32 v246, v169, v136, s85
	v_lshlrev_b32_e32 v128, 4, v128
	v_add3_u32 v247, v128, v136, s85
	v_lshl_or_b32 v249, v129, 11, v130
	v_lshl_or_b32 v248, v131, 11, v130
	v_add_u32_e32 v250, 0x40000, v248
	v_add_u32_e32 v251, 0x40000, v249
	v_add3_u32 v252, v169, v168, 0
	v_add3_u32 v253, v128, v168, 0
	s_branch .Lp1_join
.Lp1_fast:
.Lp1_join:
	ds_read_b128 v[136:139], v246 offset:0
	ds_read_b128 v[144:147], v246 offset:2048
	ds_read_b128 v[140:143], v247 offset:0
	ds_read_b128 v[148:151], v247 offset:2048
	ds_read_b128 v[152:155], v246 offset:16384
	ds_read_b128 v[160:163], v246 offset:18432
	ds_read_b128 v[156:159], v247 offset:16384
	ds_read_b128 v[164:167], v247 offset:18432
	s_add_i32 s10, s97, 0xffffff80
	s_add_i32 s11, s10, s94
	s_cmpk_eq_i32 s97, 0x880
	s_cselect_b32 s40, s37, s91
	s_cselect_b32 s10, 0, s10
	s_cselect_b32 s39, 0x80, s97
	s_cselect_b32 s38, s36, s11
	s_add_i32 s11, s91, s97
	s_add_i32 s39, s40, s39
	s_addk_i32 s11, 0xff00
	s_add_i32 s40, s40, s10
	s_mov_b32 m0, s72
	ds_read_b128 v[168:171], v252
	ds_read_b128 v[176:179], v252 offset:2048
	ds_read_b128 v[172:175], v253
	ds_read_b128 v[180:183], v253 offset:2048
	ds_read_b128 v[184:187], v252 offset:4096
	ds_read_b128 v[192:195], v252 offset:6144
	ds_read_b128 v[188:191], v253 offset:4096
	ds_read_b128 v[196:199], v253 offset:6144
	buffer_load_dwordx4 v250, s[12:15], s11 offen lds
	s_mov_b32 m0, s75
	s_nop 0
	buffer_load_dwordx4 v251, s[12:15], s11 offen lds
	s_waitcnt vmcnt(8)
	s_waitcnt lgkmcnt(0)
	s_barrier
	s_setprio 1
	s_waitcnt lgkmcnt(5)
	v_mfma_f32_16x16x128_f8f6f4 v[124:127], v[136:143], v[168:175], v[124:127]
	v_mfma_f32_16x16x128_f8f6f4 v[120:123], v[144:151], v[168:175], v[120:123]
	s_waitcnt lgkmcnt(4)
	v_mfma_f32_16x16x128_f8f6f4 v[112:115], v[136:143], v[176:183], v[112:115]
	v_mfma_f32_16x16x128_f8f6f4 v[104:107], v[144:151], v[176:183], v[104:107]
	s_waitcnt lgkmcnt(1)
	v_mfma_f32_16x16x128_f8f6f4 v[96:99], v[136:143], v[184:191], v[96:99]
	v_mfma_f32_16x16x128_f8f6f4 v[128:131], v[144:151], v[184:191], v[88:91]
	s_waitcnt lgkmcnt(0)
	v_mfma_f32_16x16x128_f8f6f4 v[200:203], v[136:143], v[192:199], v[80:83]
	v_mfma_f32_16x16x128_f8f6f4 v[204:207], v[144:151], v[192:199], v[72:75]
	s_setprio 0
	s_setprio 1
	v_mfma_f32_16x16x128_f8f6f4 v[116:119], v[152:159], v[168:175], v[116:119]
	v_mfma_f32_16x16x128_f8f6f4 v[108:111], v[160:167], v[168:175], v[108:111]
	v_mfma_f32_16x16x128_f8f6f4 v[100:103], v[152:159], v[176:183], v[100:103]
	v_mfma_f32_16x16x128_f8f6f4 v[168:171], v[160:167], v[176:183], v[92:95]
	v_mfma_f32_16x16x128_f8f6f4 v[172:175], v[152:159], v[184:191], v[84:87]
	v_mfma_f32_16x16x128_f8f6f4 v[176:179], v[160:167], v[184:191], v[76:79]
	v_mfma_f32_16x16x128_f8f6f4 v[180:183], v[152:159], v[192:199], v[68:71]
	v_mfma_f32_16x16x128_f8f6f4 v[184:187], v[160:167], v[192:199], v[64:67]
	s_setprio 0
	s_barrier
	s_mov_b32 m0, s57
	s_mov_b32 s10, s14
	s_mov_b32 s11, s15
	s_nop 1
	ds_read_b128 v[64:67], v252 offset:16384
	ds_read_b128 v[72:75], v252 offset:18432
	ds_read_b128 v[68:71], v253 offset:16384
	ds_read_b128 v[76:79], v253 offset:18432
	ds_read_b128 v[80:83], v252 offset:20480
	ds_read_b128 v[88:91], v252 offset:22528
	ds_read_b128 v[84:87], v253 offset:20480
	ds_read_b128 v[92:95], v253 offset:22528
	buffer_load_dwordx4 v244, s[8:11], s38 offen lds
	s_mov_b32 m0, s58
	s_add_i32 s41, s38, 0x40000
	buffer_load_dwordx4 v245, s[8:11], s38 offen lds
	s_mov_b32 m0, s59
	s_nop 0
	buffer_load_dwordx4 v244, s[8:11], s41 offen lds
	s_mov_b32 m0, s60
	s_nop 0
	buffer_load_dwordx4 v245, s[8:11], s41 offen lds
	s_mov_b32 m0, s56
	s_nop 0
	buffer_load_dwordx4 v248, s[12:15], s40 offen lds
	s_mov_b32 m0, s61
	s_nop 0
	buffer_load_dwordx4 v249, s[12:15], s40 offen lds
	s_waitcnt vmcnt(8)
	s_waitcnt lgkmcnt(0)
	s_barrier
	s_setprio 1
	s_waitcnt lgkmcnt(5)
	v_mfma_f32_16x16x128_f8f6f4 v[60:63], v[136:143], v[64:71], v[60:63]
	v_mfma_f32_16x16x128_f8f6f4 v[56:59], v[144:151], v[64:71], v[56:59]
	s_waitcnt lgkmcnt(4)
	v_mfma_f32_16x16x128_f8f6f4 v[48:51], v[136:143], v[72:79], v[48:51]
	v_mfma_f32_16x16x128_f8f6f4 v[188:191], v[144:151], v[72:79], v[40:43]
	s_waitcnt lgkmcnt(1)
	v_mfma_f32_16x16x128_f8f6f4 v[192:195], v[136:143], v[80:87], v[32:35]
	v_mfma_f32_16x16x128_f8f6f4 v[196:199], v[144:151], v[80:87], v[24:27]
	s_waitcnt lgkmcnt(0)
	v_mfma_f32_16x16x128_f8f6f4 v[208:211], v[136:143], v[88:95], v[16:19]
	v_mfma_f32_16x16x128_f8f6f4 v[212:215], v[144:151], v[88:95], v[8:11]
	s_setprio 0
	s_setprio 1
	v_mfma_f32_16x16x128_f8f6f4 v[52:55], v[152:159], v[64:71], v[52:55]
	v_mfma_f32_16x16x128_f8f6f4 v[216:219], v[160:167], v[64:71], v[44:47]
	v_mfma_f32_16x16x128_f8f6f4 v[220:223], v[152:159], v[72:79], v[36:39]
	v_mfma_f32_16x16x128_f8f6f4 v[224:227], v[160:167], v[72:79], v[28:31]
	v_mfma_f32_16x16x128_f8f6f4 v[228:231], v[152:159], v[80:87], v[20:23]
	v_mfma_f32_16x16x128_f8f6f4 v[232:235], v[160:167], v[80:87], v[12:15]
	v_mfma_f32_16x16x128_f8f6f4 v[236:239], v[152:159], v[88:95], v[4:7]
	v_mfma_f32_16x16x128_f8f6f4 v[240:243], v[160:167], v[88:95], v[0:3]
	s_setprio 0
	s_barrier
	s_add_i32 s41, 0, 0x18000
	s_nop 2
	s_add_i32 s41, 0, 0x1c000
	ds_read_b128 v[0:3], v246 offset:32768
	ds_read_b128 v[8:11], v246 offset:34816
	ds_read_b128 v[4:7], v247 offset:32768
	ds_read_b128 v[12:15], v247 offset:34816
	ds_read_b128 v[136:139], v246 offset:49152
	ds_read_b128 v[144:147], v246 offset:51200
	ds_read_b128 v[140:143], v247 offset:49152
	ds_read_b128 v[148:151], v247 offset:51200
	s_mov_b32 m0, s62
	ds_read_b128 v[16:19], v252 offset:32768
	ds_read_b128 v[24:27], v252 offset:34816
	ds_read_b128 v[20:23], v253 offset:32768
	ds_read_b128 v[28:31], v253 offset:34816
	ds_read_b128 v[32:35], v252 offset:36864
	ds_read_b128 v[40:43], v252 offset:38912
	ds_read_b128 v[36:39], v253 offset:36864
	ds_read_b128 v[44:47], v253 offset:38912
	buffer_load_dwordx4 v250, s[12:15], s40 offen lds
	s_mov_b32 m0, s63
	s_nop 0
	buffer_load_dwordx4 v251, s[12:15], s40 offen lds
	s_waitcnt vmcnt(8)
	s_waitcnt lgkmcnt(0)
	s_barrier
	s_setprio 1
	s_waitcnt lgkmcnt(5)
	v_mfma_f32_16x16x128_f8f6f4 v[124:127], v[0:7], v[16:23], v[124:127]
	v_mfma_f32_16x16x128_f8f6f4 v[120:123], v[8:15], v[16:23], v[120:123]
	s_waitcnt lgkmcnt(4)
	v_mfma_f32_16x16x128_f8f6f4 v[112:115], v[0:7], v[24:31], v[112:115]
	v_mfma_f32_16x16x128_f8f6f4 v[104:107], v[8:15], v[24:31], v[104:107]
	s_waitcnt lgkmcnt(1)
	v_mfma_f32_16x16x128_f8f6f4 v[96:99], v[0:7], v[32:39], v[96:99]
	v_mfma_f32_16x16x128_f8f6f4 v[88:91], v[8:15], v[32:39], v[128:131]
	s_waitcnt lgkmcnt(0)
	v_mfma_f32_16x16x128_f8f6f4 v[80:83], v[0:7], v[40:47], v[200:203]
	v_mfma_f32_16x16x128_f8f6f4 v[72:75], v[8:15], v[40:47], v[204:207]
	s_setprio 0
	s_setprio 1
	v_mfma_f32_16x16x128_f8f6f4 v[116:119], v[136:143], v[16:23], v[116:119]
	v_mfma_f32_16x16x128_f8f6f4 v[108:111], v[144:151], v[16:23], v[108:111]
	v_mfma_f32_16x16x128_f8f6f4 v[100:103], v[136:143], v[24:31], v[100:103]
	v_mfma_f32_16x16x128_f8f6f4 v[92:95], v[144:151], v[24:31], v[168:171]
	v_mfma_f32_16x16x128_f8f6f4 v[84:87], v[136:143], v[32:39], v[172:175]
	v_mfma_f32_16x16x128_f8f6f4 v[76:79], v[144:151], v[32:39], v[176:179]
	v_mfma_f32_16x16x128_f8f6f4 v[68:71], v[136:143], v[40:47], v[180:183]
	v_mfma_f32_16x16x128_f8f6f4 v[64:67], v[144:151], v[40:47], v[184:187]
	s_setprio 0
	s_barrier
	s_mov_b32 m0, s64
	s_add_i32 s40, s38, 0x80
	ds_read_b128 v[152:155], v252 offset:49152
	ds_read_b128 v[160:163], v252 offset:51200
	ds_read_b128 v[156:159], v253 offset:49152
	ds_read_b128 v[164:167], v253 offset:51200
	ds_read_b128 v[168:171], v252 offset:53248
	ds_read_b128 v[176:179], v252 offset:55296
	ds_read_b128 v[172:175], v253 offset:53248
	ds_read_b128 v[180:183], v253 offset:55296
	buffer_load_dwordx4 v244, s[8:11], s40 offen lds
	s_mov_b32 m0, s65
	s_add_i32 s38, s38, 0x40080
	buffer_load_dwordx4 v245, s[8:11], s40 offen lds
	s_mov_b32 m0, s68
	s_nop 0
	buffer_load_dwordx4 v244, s[8:11], s38 offen lds
	s_mov_b32 m0, s69
	s_nop 0
	buffer_load_dwordx4 v245, s[8:11], s38 offen lds
	s_mov_b32 m0, s66
	s_nop 0
	buffer_load_dwordx4 v248, s[12:15], s39 offen lds
	s_mov_b32 m0, s67
	s_nop 0
	buffer_load_dwordx4 v249, s[12:15], s39 offen lds
	s_waitcnt vmcnt(8)
	s_waitcnt lgkmcnt(0)
	s_barrier
	s_setprio 1
	s_waitcnt lgkmcnt(5)
	v_mfma_f32_16x16x128_f8f6f4 v[60:63], v[0:7], v[152:159], v[60:63]
	v_mfma_f32_16x16x128_f8f6f4 v[56:59], v[8:15], v[152:159], v[56:59]
	s_waitcnt lgkmcnt(4)
	v_mfma_f32_16x16x128_f8f6f4 v[48:51], v[0:7], v[160:167], v[48:51]
	v_mfma_f32_16x16x128_f8f6f4 v[40:43], v[8:15], v[160:167], v[188:191]
	s_waitcnt lgkmcnt(1)
	v_mfma_f32_16x16x128_f8f6f4 v[32:35], v[0:7], v[168:175], v[192:195]
	v_mfma_f32_16x16x128_f8f6f4 v[24:27], v[8:15], v[168:175], v[196:199]
	s_waitcnt lgkmcnt(0)
	v_mfma_f32_16x16x128_f8f6f4 v[16:19], v[0:7], v[176:183], v[208:211]
	v_mfma_f32_16x16x128_f8f6f4 v[8:11], v[8:15], v[176:183], v[212:215]
	s_setprio 0
	s_setprio 1
	v_mfma_f32_16x16x128_f8f6f4 v[52:55], v[136:143], v[152:159], v[52:55]
	v_mfma_f32_16x16x128_f8f6f4 v[44:47], v[144:151], v[152:159], v[216:219]
	v_mfma_f32_16x16x128_f8f6f4 v[36:39], v[136:143], v[160:167], v[220:223]
	v_mfma_f32_16x16x128_f8f6f4 v[28:31], v[144:151], v[160:167], v[224:227]
	v_mfma_f32_16x16x128_f8f6f4 v[20:23], v[136:143], v[168:175], v[228:231]
	v_mfma_f32_16x16x128_f8f6f4 v[12:15], v[144:151], v[168:175], v[232:235]
	v_mfma_f32_16x16x128_f8f6f4 v[4:7], v[136:143], v[176:183], v[236:239]
	v_mfma_f32_16x16x128_f8f6f4 v[0:3], v[144:151], v[176:183], v[240:243]
	s_setprio 0
	s_barrier
	s_add_i32 s96, s96, 2
	s_addk_i32 s97, 0x100
	s_cmp_gt_u32 s96, 13
	s_cbranch_scc1 .LBB0_1022

.LBB0_2173:
	s_cmpk_lg_i32 s62, 0x180
	s_cbranch_scc1 .Lp5_fast
	v_add_u32_e32 v129, s17, v128
	v_lshlrev_b32_e32 v130, 4, v128
	v_ashrrev_i32_e32 v131, 3, v129
	v_bitop3_b32 v130, v129, s22, v130 bitop3:0x48
	v_lshlrev_b32_e32 v132, 1, v131
	v_lshrrev_b32_e32 v133, 2, v131
	v_lshl_add_u32 v129, v129, 4, v134
	v_and_b32_e32 v132, 24, v132
	v_and_b32_e32 v133, 4, v133
	v_and_b32_e32 v136, 0x1fffe3, v131
	v_ashrrev_i32_e32 v129, 7, v129
	v_or3_b32 v132, v136, v133, v132
	v_lshlrev_b32_e32 v133, 1, v129
	v_lshrrev_b32_e32 v136, 2, v129
	v_and_b32_e32 v133, 24, v133
	v_and_b32_e32 v136, 4, v136
	v_and_b32_e32 v137, 0x1fffe3, v129
	v_or3_b32 v133, v137, v136, v133
	v_and_b32_e32 v136, 15, v128
	v_lshrrev_b32_e32 v137, 3, v128
	v_bfe_u32 v128, v128, 1, 3
	v_lshlrev_b32_e32 v136, 7, v136
	v_and_b32_e32 v138, 0xffffffe, v137
	v_bitop3_b32 v137, v137, v128, s48 bitop3:0x6c
	v_or_b32_e32 v168, s42, v136
	v_or_b32_e32 v136, s43, v136
	v_lshlrev_b32_e32 v169, 4, v137
	v_bitop3_b32 v128, v138, v128, 1 bitop3:0x36
	v_add3_u32 v244, v169, v136, s49
	v_lshlrev_b32_e32 v128, 4, v128
	v_add3_u32 v245, v128, v136, s49
	v_lshl_or_b32 v247, v129, 11, v130
	v_lshl_or_b32 v132, v132, 11, v130
	v_lshl_or_b32 v133, v133, 11, v130
	v_lshl_or_b32 v246, v131, 11, v130
	v_add_u32_e32 v248, 0x40000, v246
	v_add_u32_e32 v249, 0x40000, v247
	v_add3_u32 v250, v169, v168, 0
	v_add3_u32 v251, v128, v168, 0
	s_branch .Lp5_join
.Lp5_fast:
.Lp5_join:
	ds_read_b128 v[136:139], v244 offset:0
	ds_read_b128 v[144:147], v244 offset:2048
	ds_read_b128 v[140:143], v245 offset:0
	ds_read_b128 v[148:151], v245 offset:2048
	ds_read_b128 v[152:155], v244 offset:16384
	ds_read_b128 v[160:163], v244 offset:18432
	ds_read_b128 v[156:159], v245 offset:16384
	ds_read_b128 v[164:167], v245 offset:18432
	s_add_i32 s6, s62, 0xffffff80
	s_add_i32 s7, s6, s57
	s_cmpk_eq_i32 s62, 0x880
	s_cselect_b32 s65, s35, s54
	s_cselect_b32 s6, 0, s6
	s_cselect_b32 s64, 0x80, s62
	s_cselect_b32 s63, s29, s7
	s_add_i32 s7, s54, s62
	s_add_i32 s64, s65, s64
	s_addk_i32 s7, 0xff00
	s_add_i32 s65, s65, s6
	s_mov_b32 m0, s44
	ds_read_b128 v[168:171], v250
	ds_read_b128 v[176:179], v250 offset:2048
	ds_read_b128 v[172:175], v251
	ds_read_b128 v[180:183], v251 offset:2048
	ds_read_b128 v[184:187], v250 offset:4096
	ds_read_b128 v[192:195], v250 offset:6144
	ds_read_b128 v[188:191], v251 offset:4096
	ds_read_b128 v[196:199], v251 offset:6144
	buffer_load_dwordx4 v248, s[8:11], s7 offen lds
	s_mov_b32 m0, s47
	s_nop 0
	buffer_load_dwordx4 v249, s[8:11], s7 offen lds
	s_waitcnt vmcnt(8)
	s_waitcnt lgkmcnt(0)
	s_barrier
	s_setprio 1
	s_waitcnt lgkmcnt(5)
	v_mfma_f32_16x16x128_f8f6f4 v[124:127], v[136:143], v[168:175], v[124:127]
	v_mfma_f32_16x16x128_f8f6f4 v[120:123], v[144:151], v[168:175], v[120:123]
	s_waitcnt lgkmcnt(4)
	v_mfma_f32_16x16x128_f8f6f4 v[108:111], v[136:143], v[176:183], v[108:111]
	v_mfma_f32_16x16x128_f8f6f4 v[104:107], v[144:151], v[176:183], v[104:107]
	s_waitcnt lgkmcnt(1)
	v_mfma_f32_16x16x128_f8f6f4 v[128:131], v[136:143], v[184:191], v[92:95]
	v_mfma_f32_16x16x128_f8f6f4 v[200:203], v[144:151], v[184:191], v[88:91]
	s_waitcnt lgkmcnt(0)
	v_mfma_f32_16x16x128_f8f6f4 v[204:207], v[136:143], v[192:199], v[76:79]
	v_mfma_f32_16x16x128_f8f6f4 v[208:211], v[144:151], v[192:199], v[72:75]
	s_setprio 0
	s_setprio 1
	v_mfma_f32_16x16x128_f8f6f4 v[116:119], v[152:159], v[168:175], v[116:119]
	v_mfma_f32_16x16x128_f8f6f4 v[112:115], v[160:167], v[168:175], v[112:115]
	v_mfma_f32_16x16x128_f8f6f4 v[100:103], v[152:159], v[176:183], v[100:103]
	v_mfma_f32_16x16x128_f8f6f4 v[96:99], v[160:167], v[176:183], v[96:99]
	v_mfma_f32_16x16x128_f8f6f4 v[168:171], v[152:159], v[184:191], v[84:87]
	v_mfma_f32_16x16x128_f8f6f4 v[172:175], v[160:167], v[184:191], v[80:83]
	v_mfma_f32_16x16x128_f8f6f4 v[176:179], v[152:159], v[192:199], v[68:71]
	v_mfma_f32_16x16x128_f8f6f4 v[180:183], v[160:167], v[192:199], v[64:67]
	s_setprio 0
	s_barrier
	s_mov_b32 m0, s26
	s_mov_b32 s6, s10
	s_mov_b32 s7, s11
	s_nop 1
	ds_read_b128 v[64:67], v250 offset:16384
	ds_read_b128 v[72:75], v250 offset:18432
	ds_read_b128 v[68:71], v251 offset:16384
	ds_read_b128 v[76:79], v251 offset:18432
	ds_read_b128 v[80:83], v250 offset:20480
	ds_read_b128 v[88:91], v250 offset:22528
	ds_read_b128 v[84:87], v251 offset:20480
	ds_read_b128 v[92:95], v251 offset:22528
	buffer_load_dwordx4 v132, s[4:7], s63 offen lds
	s_mov_b32 m0, s27
	s_add_i32 s66, s63, 0x40000
	buffer_load_dwordx4 v133, s[4:7], s63 offen lds
	s_mov_b32 m0, s28
	s_nop 0
	buffer_load_dwordx4 v132, s[4:7], s66 offen lds
	s_mov_b32 m0, s30
	s_nop 0
	buffer_load_dwordx4 v133, s[4:7], s66 offen lds
	s_mov_b32 m0, s25
	s_nop 0
	buffer_load_dwordx4 v246, s[8:11], s65 offen lds
	s_mov_b32 m0, s31
	s_nop 0
	buffer_load_dwordx4 v247, s[8:11], s65 offen lds
	s_waitcnt vmcnt(8)
	s_waitcnt lgkmcnt(0)
	s_barrier
	s_setprio 1
	s_waitcnt lgkmcnt(5)
	v_mfma_f32_16x16x128_f8f6f4 v[60:63], v[136:143], v[64:71], v[60:63]
	v_mfma_f32_16x16x128_f8f6f4 v[56:59], v[144:151], v[64:71], v[56:59]
	s_waitcnt lgkmcnt(4)
	v_mfma_f32_16x16x128_f8f6f4 v[184:187], v[136:143], v[72:79], v[44:47]
	v_mfma_f32_16x16x128_f8f6f4 v[188:191], v[144:151], v[72:79], v[40:43]
	s_waitcnt lgkmcnt(1)
	v_mfma_f32_16x16x128_f8f6f4 v[192:195], v[136:143], v[80:87], v[28:31]
	v_mfma_f32_16x16x128_f8f6f4 v[196:199], v[144:151], v[80:87], v[24:27]
	s_waitcnt lgkmcnt(0)
	v_mfma_f32_16x16x128_f8f6f4 v[212:215], v[136:143], v[88:95], v[12:15]
	v_mfma_f32_16x16x128_f8f6f4 v[216:219], v[144:151], v[88:95], v[8:11]
	s_setprio 0
	s_setprio 1
	v_mfma_f32_16x16x128_f8f6f4 v[52:55], v[152:159], v[64:71], v[52:55]
	v_mfma_f32_16x16x128_f8f6f4 v[48:51], v[160:167], v[64:71], v[48:51]
	v_mfma_f32_16x16x128_f8f6f4 v[220:223], v[152:159], v[72:79], v[36:39]
	v_mfma_f32_16x16x128_f8f6f4 v[224:227], v[160:167], v[72:79], v[32:35]
	v_mfma_f32_16x16x128_f8f6f4 v[228:231], v[152:159], v[80:87], v[20:23]
	v_mfma_f32_16x16x128_f8f6f4 v[232:235], v[160:167], v[80:87], v[16:19]
	v_mfma_f32_16x16x128_f8f6f4 v[236:239], v[152:159], v[88:95], v[4:7]
	v_mfma_f32_16x16x128_f8f6f4 v[240:243], v[160:167], v[88:95], v[0:3]
	s_setprio 0
	s_barrier
	s_add_i32 s66, 0, 0x18000
	s_nop 2
	s_add_i32 s66, 0, 0x1c000
	ds_read_b128 v[0:3], v244 offset:32768
	ds_read_b128 v[16:19], v244 offset:34816
	ds_read_b128 v[4:7], v245 offset:32768
	ds_read_b128 v[20:23], v245 offset:34816
	ds_read_b128 v[136:139], v244 offset:49152
	ds_read_b128 v[144:147], v244 offset:51200
	ds_read_b128 v[140:143], v245 offset:49152
	ds_read_b128 v[148:151], v245 offset:51200
	s_mov_b32 m0, s33
	ds_read_b128 v[8:11], v250 offset:32768
	ds_read_b128 v[24:27], v250 offset:34816
	ds_read_b128 v[12:15], v251 offset:32768
	ds_read_b128 v[28:31], v251 offset:34816
	ds_read_b128 v[32:35], v250 offset:36864
	ds_read_b128 v[40:43], v250 offset:38912
	ds_read_b128 v[36:39], v251 offset:36864
	ds_read_b128 v[44:47], v251 offset:38912
	buffer_load_dwordx4 v248, s[8:11], s65 offen lds
	s_mov_b32 m0, s34
	s_nop 0
	buffer_load_dwordx4 v249, s[8:11], s65 offen lds
	s_waitcnt vmcnt(8)
	s_waitcnt lgkmcnt(0)
	s_barrier
	s_setprio 1
	s_waitcnt lgkmcnt(5)
	v_mfma_f32_16x16x128_f8f6f4 v[124:127], v[0:7], v[8:15], v[124:127]
	v_mfma_f32_16x16x128_f8f6f4 v[120:123], v[16:23], v[8:15], v[120:123]
	s_waitcnt lgkmcnt(4)
	v_mfma_f32_16x16x128_f8f6f4 v[108:111], v[0:7], v[24:31], v[108:111]
	v_mfma_f32_16x16x128_f8f6f4 v[104:107], v[16:23], v[24:31], v[104:107]
	s_waitcnt lgkmcnt(1)
	v_mfma_f32_16x16x128_f8f6f4 v[92:95], v[0:7], v[32:39], v[128:131]
	v_mfma_f32_16x16x128_f8f6f4 v[88:91], v[16:23], v[32:39], v[200:203]
	s_waitcnt lgkmcnt(0)
	v_mfma_f32_16x16x128_f8f6f4 v[76:79], v[0:7], v[40:47], v[204:207]
	v_mfma_f32_16x16x128_f8f6f4 v[72:75], v[16:23], v[40:47], v[208:211]
	s_setprio 0
	s_setprio 1
	v_mfma_f32_16x16x128_f8f6f4 v[116:119], v[136:143], v[8:15], v[116:119]
	v_mfma_f32_16x16x128_f8f6f4 v[112:115], v[144:151], v[8:15], v[112:115]
	v_mfma_f32_16x16x128_f8f6f4 v[100:103], v[136:143], v[24:31], v[100:103]
	v_mfma_f32_16x16x128_f8f6f4 v[96:99], v[144:151], v[24:31], v[96:99]
	v_mfma_f32_16x16x128_f8f6f4 v[84:87], v[136:143], v[32:39], v[168:171]
	v_mfma_f32_16x16x128_f8f6f4 v[80:83], v[144:151], v[32:39], v[172:175]
	v_mfma_f32_16x16x128_f8f6f4 v[68:71], v[136:143], v[40:47], v[176:179]
	v_mfma_f32_16x16x128_f8f6f4 v[64:67], v[144:151], v[40:47], v[180:183]
	s_setprio 0
	s_barrier
	s_mov_b32 m0, s36
	s_add_i32 s65, s63, 0x80
	ds_read_b128 v[32:35], v250 offset:49152
	ds_read_b128 v[152:155], v250 offset:51200
	ds_read_b128 v[36:39], v251 offset:49152
	ds_read_b128 v[156:159], v251 offset:51200
	ds_read_b128 v[160:163], v250 offset:53248
	ds_read_b128 v[168:171], v250 offset:55296
	ds_read_b128 v[164:167], v251 offset:53248
	ds_read_b128 v[172:175], v251 offset:55296
	buffer_load_dwordx4 v132, s[4:7], s65 offen lds
	s_mov_b32 m0, s37
	s_add_i32 s63, s63, 0x40080
	buffer_load_dwordx4 v133, s[4:7], s65 offen lds
	s_mov_b32 m0, s40
	s_nop 0
	buffer_load_dwordx4 v132, s[4:7], s63 offen lds
	s_mov_b32 m0, s41
	s_nop 0
	buffer_load_dwordx4 v133, s[4:7], s63 offen lds
	s_mov_b32 m0, s38
	s_nop 0
	buffer_load_dwordx4 v246, s[8:11], s64 offen lds
	s_mov_b32 m0, s39
	s_nop 0
	buffer_load_dwordx4 v247, s[8:11], s64 offen lds
	s_waitcnt vmcnt(8)
	s_waitcnt lgkmcnt(0)
	s_barrier
	s_setprio 1
	s_waitcnt lgkmcnt(5)
	v_mfma_f32_16x16x128_f8f6f4 v[60:63], v[0:7], v[32:39], v[60:63]
	v_mfma_f32_16x16x128_f8f6f4 v[56:59], v[16:23], v[32:39], v[56:59]
	s_waitcnt lgkmcnt(4)
	v_mfma_f32_16x16x128_f8f6f4 v[44:47], v[0:7], v[152:159], v[184:187]
	v_mfma_f32_16x16x128_f8f6f4 v[40:43], v[16:23], v[152:159], v[188:191]
	s_waitcnt lgkmcnt(1)
	v_mfma_f32_16x16x128_f8f6f4 v[28:31], v[0:7], v[160:167], v[192:195]
	v_mfma_f32_16x16x128_f8f6f4 v[24:27], v[16:23], v[160:167], v[196:199]
	s_waitcnt lgkmcnt(0)
	v_mfma_f32_16x16x128_f8f6f4 v[12:15], v[0:7], v[168:175], v[212:215]
	v_mfma_f32_16x16x128_f8f6f4 v[8:11], v[16:23], v[168:175], v[216:219]
	s_setprio 0
	s_setprio 1
	v_mfma_f32_16x16x128_f8f6f4 v[52:55], v[136:143], v[32:39], v[52:55]
	v_mfma_f32_16x16x128_f8f6f4 v[48:51], v[144:151], v[32:39], v[48:51]
	v_mfma_f32_16x16x128_f8f6f4 v[36:39], v[136:143], v[152:159], v[220:223]
	v_mfma_f32_16x16x128_f8f6f4 v[32:35], v[144:151], v[152:159], v[224:227]
	v_mfma_f32_16x16x128_f8f6f4 v[20:23], v[136:143], v[160:167], v[228:231]
	v_mfma_f32_16x16x128_f8f6f4 v[16:19], v[144:151], v[160:167], v[232:235]
	v_mfma_f32_16x16x128_f8f6f4 v[4:7], v[136:143], v[168:175], v[236:239]
	v_mfma_f32_16x16x128_f8f6f4 v[0:3], v[144:151], v[168:175], v[240:243]
	s_setprio 0
	s_barrier
	s_add_i32 s61, s61, 2
	s_addk_i32 s62, 0x100
	s_cmp_gt_u32 s61, 13
	s_cbranch_scc1 .LBB0_2177

.LBB0_2197:
	s_cmpk_lg_i32 s64, 0x180
	s_cbranch_scc1 .Lp6_fast
	v_add_u32_e32 v129, s19, v128
	v_ashrrev_i32_e32 v131, 3, v129
	v_lshlrev_b32_e32 v130, 4, v128
	v_lshlrev_b32_e32 v132, 1, v131
	v_lshrrev_b32_e32 v133, 2, v131
	v_bitop3_b32 v130, v129, s24, v130 bitop3:0x48
	v_and_b32_e32 v132, 24, v132
	v_and_b32_e32 v133, 4, v133
	v_and_b32_e32 v134, 0x1fffe3, v131
	v_lshl_add_u32 v129, v129, 4, v156
	v_or3_b32 v132, v134, v133, v132
	v_ashrrev_i32_e32 v129, 7, v129
	v_lshl_or_b32 v159, v132, 11, v130
	v_lshlrev_b32_e32 v132, 1, v129
	v_lshrrev_b32_e32 v133, 2, v129
	v_and_b32_e32 v132, 24, v132
	v_and_b32_e32 v133, 4, v133
	v_and_b32_e32 v134, 0x1fffe3, v129
	v_or3_b32 v132, v134, v133, v132
	v_lshrrev_b32_e32 v133, 3, v128
	v_lshl_or_b32 v244, v132, 11, v130
	v_and_b32_e32 v132, 15, v128
	v_and_b32_e32 v134, 0xffffffe, v133
	v_bfe_u32 v128, v128, 1, 3
	v_lshlrev_b32_e32 v132, 7, v132
	v_bitop3_b32 v133, v133, v128, s50 bitop3:0x6c
	v_bitop3_b32 v128, v134, v128, 1 bitop3:0x36
	v_or_b32_e32 v152, s44, v132
	v_or_b32_e32 v132, s45, v132
	v_lshlrev_b32_e32 v153, 4, v133
	v_lshlrev_b32_e32 v154, 4, v128
	v_add3_u32 v245, v153, v132, s51
	v_add3_u32 v246, v154, v132, s51
	v_lshl_or_b32 v247, v131, 11, v130
	v_lshl_or_b32 v248, v129, 11, v130
	v_add_u32_e32 v249, 0x40000, v247
	v_add_u32_e32 v250, 0x40000, v248
	v_add3_u32 v251, v153, v152, 0
	v_add3_u32 v252, v154, v152, 0
	s_branch .Lp6_join
.Lp6_fast:
.Lp6_join:
	ds_read_b128 v[128:131], v245 offset:0
	ds_read_b128 v[136:139], v245 offset:2048
	ds_read_b128 v[132:135], v246 offset:0
	ds_read_b128 v[140:143], v246 offset:2048
	ds_read_b128 v[144:147], v245 offset:16384
	ds_read_b128 v[160:163], v245 offset:18432
	ds_read_b128 v[148:151], v246 offset:16384
	ds_read_b128 v[164:167], v246 offset:18432
	s_add_i32 s6, s64, 0xffffff80
	s_add_i32 s7, s6, s59
	s_cmpk_eq_i32 s64, 0x880
	s_cselect_b32 s67, s37, s56
	s_cselect_b32 s6, 0, s6
	s_cselect_b32 s66, 0x80, s64
	s_cselect_b32 s65, s31, s7
	s_add_i32 s7, s56, s64
	s_add_i32 s66, s67, s66
	s_addk_i32 s7, 0xff00
	s_add_i32 s67, s67, s6
	s_mov_b32 m0, s46
	ds_read_b128 v[168:171], v251
	ds_read_b128 v[176:179], v251 offset:2048
	ds_read_b128 v[172:175], v252
	ds_read_b128 v[180:183], v252 offset:2048
	ds_read_b128 v[184:187], v251 offset:4096
	ds_read_b128 v[192:195], v251 offset:6144
	ds_read_b128 v[188:191], v252 offset:4096
	ds_read_b128 v[196:199], v252 offset:6144
	buffer_load_dwordx4 v249, s[8:11], s7 offen lds
	s_mov_b32 m0, s49
	s_nop 0
	buffer_load_dwordx4 v250, s[8:11], s7 offen lds
	s_waitcnt vmcnt(8)
	s_waitcnt lgkmcnt(0)
	s_barrier
	s_setprio 1
	s_waitcnt lgkmcnt(5)
	v_mfma_f32_16x16x128_f8f6f4 v[124:127], v[128:135], v[168:175], v[124:127]
	v_mfma_f32_16x16x128_f8f6f4 v[120:123], v[136:143], v[168:175], v[120:123]
	s_waitcnt lgkmcnt(4)
	v_mfma_f32_16x16x128_f8f6f4 v[108:111], v[128:135], v[176:183], v[108:111]
	v_mfma_f32_16x16x128_f8f6f4 v[104:107], v[136:143], v[176:183], v[104:107]
	s_waitcnt lgkmcnt(1)
	v_mfma_f32_16x16x128_f8f6f4 v[152:155], v[128:135], v[184:191], v[92:95]
	v_mfma_f32_16x16x128_f8f6f4 v[200:203], v[136:143], v[184:191], v[88:91]
	s_waitcnt lgkmcnt(0)
	v_mfma_f32_16x16x128_f8f6f4 v[204:207], v[128:135], v[192:199], v[76:79]
	v_mfma_f32_16x16x128_f8f6f4 v[208:211], v[136:143], v[192:199], v[72:75]
	s_setprio 0
	s_setprio 1
	v_mfma_f32_16x16x128_f8f6f4 v[116:119], v[144:151], v[168:175], v[116:119]
	v_mfma_f32_16x16x128_f8f6f4 v[112:115], v[160:167], v[168:175], v[112:115]
	v_mfma_f32_16x16x128_f8f6f4 v[100:103], v[144:151], v[176:183], v[100:103]
	v_mfma_f32_16x16x128_f8f6f4 v[96:99], v[160:167], v[176:183], v[96:99]
	v_mfma_f32_16x16x128_f8f6f4 v[168:171], v[144:151], v[184:191], v[84:87]
	v_mfma_f32_16x16x128_f8f6f4 v[172:175], v[160:167], v[184:191], v[80:83]
	v_mfma_f32_16x16x128_f8f6f4 v[176:179], v[144:151], v[192:199], v[68:71]
	v_mfma_f32_16x16x128_f8f6f4 v[180:183], v[160:167], v[192:199], v[64:67]
	s_setprio 0
	s_barrier
	s_mov_b32 m0, s28
	s_mov_b32 s6, s10
	s_mov_b32 s7, s11
	s_nop 1
	ds_read_b128 v[64:67], v251 offset:16384
	ds_read_b128 v[72:75], v251 offset:18432
	ds_read_b128 v[68:71], v252 offset:16384
	ds_read_b128 v[76:79], v252 offset:18432
	ds_read_b128 v[80:83], v251 offset:20480
	ds_read_b128 v[88:91], v251 offset:22528
	ds_read_b128 v[84:87], v252 offset:20480
	ds_read_b128 v[92:95], v252 offset:22528
	buffer_load_dwordx4 v159, s[4:7], s65 offen lds
	s_mov_b32 m0, s29
	s_add_i32 s68, s65, 0x40000
	buffer_load_dwordx4 v244, s[4:7], s65 offen lds
	s_mov_b32 m0, s30
	s_nop 0
	buffer_load_dwordx4 v159, s[4:7], s68 offen lds
	s_mov_b32 m0, s33
	s_nop 0
	buffer_load_dwordx4 v244, s[4:7], s68 offen lds
	s_mov_b32 m0, s27
	s_nop 0
	buffer_load_dwordx4 v247, s[8:11], s67 offen lds
	s_mov_b32 m0, s34
	s_nop 0
	buffer_load_dwordx4 v248, s[8:11], s67 offen lds
	s_waitcnt vmcnt(8)
	s_waitcnt lgkmcnt(0)
	s_barrier
	s_setprio 1
	s_waitcnt lgkmcnt(5)
	v_mfma_f32_16x16x128_f8f6f4 v[60:63], v[128:135], v[64:71], v[60:63]
	v_mfma_f32_16x16x128_f8f6f4 v[56:59], v[136:143], v[64:71], v[56:59]
	s_waitcnt lgkmcnt(4)
	v_mfma_f32_16x16x128_f8f6f4 v[184:187], v[128:135], v[72:79], v[44:47]
	v_mfma_f32_16x16x128_f8f6f4 v[188:191], v[136:143], v[72:79], v[40:43]
	s_waitcnt lgkmcnt(1)
	v_mfma_f32_16x16x128_f8f6f4 v[192:195], v[128:135], v[80:87], v[28:31]
	v_mfma_f32_16x16x128_f8f6f4 v[196:199], v[136:143], v[80:87], v[24:27]
	s_waitcnt lgkmcnt(0)
	v_mfma_f32_16x16x128_f8f6f4 v[212:215], v[128:135], v[88:95], v[12:15]
	v_mfma_f32_16x16x128_f8f6f4 v[216:219], v[136:143], v[88:95], v[8:11]
	s_setprio 0
	s_setprio 1
	v_mfma_f32_16x16x128_f8f6f4 v[52:55], v[144:151], v[64:71], v[52:55]
	v_mfma_f32_16x16x128_f8f6f4 v[48:51], v[160:167], v[64:71], v[48:51]
	v_mfma_f32_16x16x128_f8f6f4 v[220:223], v[144:151], v[72:79], v[36:39]
	v_mfma_f32_16x16x128_f8f6f4 v[224:227], v[160:167], v[72:79], v[32:35]
	v_mfma_f32_16x16x128_f8f6f4 v[228:231], v[144:151], v[80:87], v[20:23]
	v_mfma_f32_16x16x128_f8f6f4 v[232:235], v[160:167], v[80:87], v[16:19]
	v_mfma_f32_16x16x128_f8f6f4 v[236:239], v[144:151], v[88:95], v[4:7]
	v_mfma_f32_16x16x128_f8f6f4 v[240:243], v[160:167], v[88:95], v[0:3]
	s_setprio 0
	s_barrier
	s_add_i32 s68, 0, 0x18000
	s_nop 2
	s_add_i32 s68, 0, 0x1c000
	ds_read_b128 v[0:3], v245 offset:32768
	ds_read_b128 v[16:19], v245 offset:34816
	ds_read_b128 v[4:7], v246 offset:32768
	ds_read_b128 v[20:23], v246 offset:34816
	ds_read_b128 v[128:131], v245 offset:49152
	ds_read_b128 v[136:139], v245 offset:51200
	ds_read_b128 v[132:135], v246 offset:49152
	ds_read_b128 v[140:143], v246 offset:51200
	s_mov_b32 m0, s35
	ds_read_b128 v[8:11], v251 offset:32768
	ds_read_b128 v[24:27], v251 offset:34816
	ds_read_b128 v[12:15], v252 offset:32768
	ds_read_b128 v[28:31], v252 offset:34816
	ds_read_b128 v[32:35], v251 offset:36864
	ds_read_b128 v[40:43], v251 offset:38912
	ds_read_b128 v[36:39], v252 offset:36864
	ds_read_b128 v[44:47], v252 offset:38912
	buffer_load_dwordx4 v249, s[8:11], s67 offen lds
	s_mov_b32 m0, s36
	s_nop 0
	buffer_load_dwordx4 v250, s[8:11], s67 offen lds
	s_waitcnt vmcnt(8)
	s_waitcnt lgkmcnt(0)
	s_barrier
	s_setprio 1
	s_waitcnt lgkmcnt(5)
	v_mfma_f32_16x16x128_f8f6f4 v[124:127], v[0:7], v[8:15], v[124:127]
	v_mfma_f32_16x16x128_f8f6f4 v[120:123], v[16:23], v[8:15], v[120:123]
	s_waitcnt lgkmcnt(4)
	v_mfma_f32_16x16x128_f8f6f4 v[108:111], v[0:7], v[24:31], v[108:111]
	v_mfma_f32_16x16x128_f8f6f4 v[104:107], v[16:23], v[24:31], v[104:107]
	s_waitcnt lgkmcnt(1)
	v_mfma_f32_16x16x128_f8f6f4 v[92:95], v[0:7], v[32:39], v[152:155]
	v_mfma_f32_16x16x128_f8f6f4 v[88:91], v[16:23], v[32:39], v[200:203]
	s_waitcnt lgkmcnt(0)
	v_mfma_f32_16x16x128_f8f6f4 v[76:79], v[0:7], v[40:47], v[204:207]
	v_mfma_f32_16x16x128_f8f6f4 v[72:75], v[16:23], v[40:47], v[208:211]
	s_setprio 0
	s_setprio 1
	v_mfma_f32_16x16x128_f8f6f4 v[116:119], v[128:135], v[8:15], v[116:119]
	v_mfma_f32_16x16x128_f8f6f4 v[112:115], v[136:143], v[8:15], v[112:115]
	v_mfma_f32_16x16x128_f8f6f4 v[100:103], v[128:135], v[24:31], v[100:103]
	v_mfma_f32_16x16x128_f8f6f4 v[96:99], v[136:143], v[24:31], v[96:99]
	v_mfma_f32_16x16x128_f8f6f4 v[84:87], v[128:135], v[32:39], v[168:171]
	v_mfma_f32_16x16x128_f8f6f4 v[80:83], v[136:143], v[32:39], v[172:175]
	v_mfma_f32_16x16x128_f8f6f4 v[68:71], v[128:135], v[40:47], v[176:179]
	v_mfma_f32_16x16x128_f8f6f4 v[64:67], v[136:143], v[40:47], v[180:183]
	s_setprio 0
	s_barrier
	s_mov_b32 m0, s38
	s_add_i32 s67, s65, 0x80
	ds_read_b128 v[32:35], v251 offset:49152
	ds_read_b128 v[144:147], v251 offset:51200
	ds_read_b128 v[36:39], v252 offset:49152
	ds_read_b128 v[148:151], v252 offset:51200
	ds_read_b128 v[160:163], v251 offset:53248
	ds_read_b128 v[168:171], v251 offset:55296
	ds_read_b128 v[164:167], v252 offset:53248
	ds_read_b128 v[172:175], v252 offset:55296
	buffer_load_dwordx4 v159, s[4:7], s67 offen lds
	s_mov_b32 m0, s39
	s_add_i32 s65, s65, 0x40080
	buffer_load_dwordx4 v244, s[4:7], s67 offen lds
	s_mov_b32 m0, s42
	s_nop 0
	buffer_load_dwordx4 v159, s[4:7], s65 offen lds
	s_mov_b32 m0, s43
	s_nop 0
	buffer_load_dwordx4 v244, s[4:7], s65 offen lds
	s_mov_b32 m0, s40
	s_nop 0
	buffer_load_dwordx4 v247, s[8:11], s66 offen lds
	s_mov_b32 m0, s41
	s_nop 0
	buffer_load_dwordx4 v248, s[8:11], s66 offen lds
	s_waitcnt vmcnt(8)
	s_waitcnt lgkmcnt(0)
	s_barrier
	s_setprio 1
	s_waitcnt lgkmcnt(5)
	v_mfma_f32_16x16x128_f8f6f4 v[60:63], v[0:7], v[32:39], v[60:63]
	v_mfma_f32_16x16x128_f8f6f4 v[56:59], v[16:23], v[32:39], v[56:59]
	s_waitcnt lgkmcnt(4)
	v_mfma_f32_16x16x128_f8f6f4 v[44:47], v[0:7], v[144:151], v[184:187]
	v_mfma_f32_16x16x128_f8f6f4 v[40:43], v[16:23], v[144:151], v[188:191]
	s_waitcnt lgkmcnt(1)
	v_mfma_f32_16x16x128_f8f6f4 v[28:31], v[0:7], v[160:167], v[192:195]
	v_mfma_f32_16x16x128_f8f6f4 v[24:27], v[16:23], v[160:167], v[196:199]
	s_waitcnt lgkmcnt(0)
	v_mfma_f32_16x16x128_f8f6f4 v[12:15], v[0:7], v[168:175], v[212:215]
	v_mfma_f32_16x16x128_f8f6f4 v[8:11], v[16:23], v[168:175], v[216:219]
	s_setprio 0
	s_setprio 1
	v_mfma_f32_16x16x128_f8f6f4 v[52:55], v[128:135], v[32:39], v[52:55]
	v_mfma_f32_16x16x128_f8f6f4 v[48:51], v[136:143], v[32:39], v[48:51]
	v_mfma_f32_16x16x128_f8f6f4 v[36:39], v[128:135], v[144:151], v[220:223]
	v_mfma_f32_16x16x128_f8f6f4 v[32:35], v[136:143], v[144:151], v[224:227]
	v_mfma_f32_16x16x128_f8f6f4 v[20:23], v[128:135], v[160:167], v[228:231]
	v_mfma_f32_16x16x128_f8f6f4 v[16:19], v[136:143], v[160:167], v[232:235]
	v_mfma_f32_16x16x128_f8f6f4 v[4:7], v[128:135], v[168:175], v[236:239]
	v_mfma_f32_16x16x128_f8f6f4 v[0:3], v[136:143], v[168:175], v[240:243]
	s_setprio 0
	s_barrier
	s_add_i32 s63, s63, 2
	s_addk_i32 s64, 0x100
	s_cmp_gt_u32 s63, 13
	s_cbranch_scc1 .LBB0_2201

.LBB0_2275:
	s_cmpk_lg_i32 s61, 0x180
	s_cbranch_scc1 .Lp7_fast
	v_add_u32_e32 v129, s17, v128
	v_ashrrev_i32_e32 v131, 3, v129
	v_lshlrev_b32_e32 v130, 4, v128
	v_lshlrev_b32_e32 v132, 1, v131
	v_lshrrev_b32_e32 v133, 2, v131
	v_bitop3_b32 v130, v129, s22, v130 bitop3:0x48
	v_and_b32_e32 v132, 24, v132
	v_and_b32_e32 v133, 4, v133
	v_and_b32_e32 v134, 0x1fffe3, v131
	v_lshl_add_u32 v129, v129, 4, v136
	v_or3_b32 v132, v134, v133, v132
	v_ashrrev_i32_e32 v129, 7, v129
	v_lshl_or_b32 v242, v132, 11, v130
	v_lshlrev_b32_e32 v132, 1, v129
	v_lshrrev_b32_e32 v133, 2, v129
	v_and_b32_e32 v132, 24, v132
	v_and_b32_e32 v133, 4, v133
	v_and_b32_e32 v134, 0x1fffe3, v129
	v_or3_b32 v132, v134, v133, v132
	v_lshrrev_b32_e32 v133, 3, v128
	v_lshl_or_b32 v243, v132, 11, v130
	v_and_b32_e32 v132, 15, v128
	v_and_b32_e32 v134, 0xffffffe, v133
	v_bfe_u32 v128, v128, 1, 3
	v_lshlrev_b32_e32 v132, 7, v132
	v_bitop3_b32 v133, v133, v128, s48 bitop3:0x6c
	v_bitop3_b32 v128, v134, v128, 1 bitop3:0x36
	v_or_b32_e32 v162, s42, v132
	v_or_b32_e32 v132, s43, v132
	v_lshlrev_b32_e32 v163, 4, v133
	v_lshlrev_b32_e32 v164, 4, v128
	v_add3_u32 v244, v163, v132, s49
	v_add3_u32 v245, v164, v132, s49
	v_lshl_or_b32 v246, v131, 11, v130
	v_lshl_or_b32 v247, v129, 11, v130
	v_add_u32_e32 v248, 0x40000, v246
	v_add_u32_e32 v249, 0x40000, v247
	v_add3_u32 v250, v163, v162, 0
	v_add3_u32 v251, v164, v162, 0
	s_branch .Lp7_join
.Lp7_fast:
.Lp7_join:
	ds_read_b128 v[128:131], v244 offset:0
	ds_read_b128 v[138:141], v244 offset:2048
	ds_read_b128 v[132:135], v245 offset:0
	ds_read_b128 v[142:145], v245 offset:2048
	ds_read_b128 v[146:149], v244 offset:16384
	ds_read_b128 v[154:157], v244 offset:18432
	ds_read_b128 v[150:153], v245 offset:16384
	ds_read_b128 v[158:161], v245 offset:18432
	s_add_i32 s6, s61, 0xffffff80
	s_add_i32 s7, s6, s56
	s_cmpk_eq_i32 s61, 0x880
	s_cselect_b32 s64, s35, s53
	s_cselect_b32 s6, 0, s6
	s_cselect_b32 s63, 0x80, s61
	s_cselect_b32 s62, s29, s7
	s_add_i32 s7, s53, s61
	s_add_i32 s63, s64, s63
	s_addk_i32 s7, 0xff00
	s_add_i32 s64, s64, s6
	s_mov_b32 m0, s44
	ds_read_b128 v[162:165], v250
	ds_read_b128 v[170:173], v250 offset:2048
	ds_read_b128 v[166:169], v251
	ds_read_b128 v[174:177], v251 offset:2048
	ds_read_b128 v[178:181], v250 offset:4096
	ds_read_b128 v[186:189], v250 offset:6144
	ds_read_b128 v[182:185], v251 offset:4096
	ds_read_b128 v[190:193], v251 offset:6144
	buffer_load_dwordx4 v248, s[8:11], s7 offen lds
	s_mov_b32 m0, s47
	s_nop 0
	buffer_load_dwordx4 v249, s[8:11], s7 offen lds
	s_waitcnt vmcnt(8)
	s_waitcnt lgkmcnt(0)
	s_barrier
	s_setprio 1
	s_waitcnt lgkmcnt(0)
	v_mfma_f32_16x16x128_f8f6f4 v[124:127], v[128:135], v[162:169], v[124:127]
	v_mfma_f32_16x16x128_f8f6f4 v[120:123], v[138:145], v[162:169], v[120:123]
	v_mfma_f32_16x16x128_f8f6f4 v[116:119], v[128:135], v[170:177], v[116:119]
	v_mfma_f32_16x16x128_f8f6f4 v[112:115], v[138:145], v[170:177], v[112:115]
	v_mfma_f32_16x16x128_f8f6f4 v[194:197], v[128:135], v[178:185], v[92:95]
	v_mfma_f32_16x16x128_f8f6f4 v[198:201], v[138:145], v[178:185], v[88:91]
	v_mfma_f32_16x16x128_f8f6f4 v[202:205], v[128:135], v[186:193], v[84:87]
	v_mfma_f32_16x16x128_f8f6f4 v[206:209], v[138:145], v[186:193], v[80:83]
	s_setprio 0
	s_setprio 1
	v_mfma_f32_16x16x128_f8f6f4 v[108:111], v[146:153], v[162:169], v[108:111]
	v_mfma_f32_16x16x128_f8f6f4 v[104:107], v[154:161], v[162:169], v[104:107]
	v_mfma_f32_16x16x128_f8f6f4 v[100:103], v[146:153], v[170:177], v[100:103]
	v_mfma_f32_16x16x128_f8f6f4 v[96:99], v[154:161], v[170:177], v[96:99]
	v_mfma_f32_16x16x128_f8f6f4 v[162:165], v[146:153], v[178:185], v[76:79]
	v_mfma_f32_16x16x128_f8f6f4 v[166:169], v[154:161], v[178:185], v[72:75]
	v_mfma_f32_16x16x128_f8f6f4 v[170:173], v[146:153], v[186:193], v[68:71]
	v_mfma_f32_16x16x128_f8f6f4 v[174:177], v[154:161], v[186:193], v[64:67]
	s_setprio 0
	s_barrier
	s_mov_b32 m0, s26
	s_mov_b32 s6, s10
	s_mov_b32 s7, s11
	s_nop 1
	ds_read_b128 v[64:67], v250 offset:16384
	ds_read_b128 v[72:75], v250 offset:18432
	ds_read_b128 v[68:71], v251 offset:16384
	ds_read_b128 v[76:79], v251 offset:18432
	ds_read_b128 v[80:83], v250 offset:20480
	ds_read_b128 v[88:91], v250 offset:22528
	ds_read_b128 v[84:87], v251 offset:20480
	ds_read_b128 v[92:95], v251 offset:22528
	buffer_load_dwordx4 v242, s[4:7], s62 offen lds
	s_mov_b32 m0, s27
	s_add_i32 s65, s62, 0x40000
	buffer_load_dwordx4 v243, s[4:7], s62 offen lds
	s_mov_b32 m0, s28
	s_nop 0
	buffer_load_dwordx4 v242, s[4:7], s65 offen lds
	s_mov_b32 m0, s30
	s_nop 0
	buffer_load_dwordx4 v243, s[4:7], s65 offen lds
	s_mov_b32 m0, s25
	s_nop 0
	buffer_load_dwordx4 v246, s[8:11], s64 offen lds
	s_mov_b32 m0, s31
	s_nop 0
	buffer_load_dwordx4 v247, s[8:11], s64 offen lds
	s_waitcnt vmcnt(8)
	s_waitcnt lgkmcnt(0)
	s_barrier
	s_setprio 1
	s_waitcnt lgkmcnt(5)
	v_mfma_f32_16x16x128_f8f6f4 v[60:63], v[128:135], v[64:71], v[60:63]
	v_mfma_f32_16x16x128_f8f6f4 v[56:59], v[138:145], v[64:71], v[56:59]
	s_waitcnt lgkmcnt(4)
	v_mfma_f32_16x16x128_f8f6f4 v[52:55], v[128:135], v[72:79], v[52:55]
	v_mfma_f32_16x16x128_f8f6f4 v[48:51], v[138:145], v[72:79], v[48:51]
	s_waitcnt lgkmcnt(1)
	v_mfma_f32_16x16x128_f8f6f4 v[178:181], v[128:135], v[80:87], v[28:31]
	v_mfma_f32_16x16x128_f8f6f4 v[182:185], v[138:145], v[80:87], v[24:27]
	s_waitcnt lgkmcnt(0)
	v_mfma_f32_16x16x128_f8f6f4 v[186:189], v[128:135], v[88:95], v[20:23]
	v_mfma_f32_16x16x128_f8f6f4 v[190:193], v[138:145], v[88:95], v[16:19]
	s_setprio 0
	s_setprio 1
	v_mfma_f32_16x16x128_f8f6f4 v[210:213], v[146:153], v[64:71], v[44:47]
	v_mfma_f32_16x16x128_f8f6f4 v[214:217], v[154:161], v[64:71], v[40:43]
	v_mfma_f32_16x16x128_f8f6f4 v[218:221], v[146:153], v[72:79], v[36:39]
	v_mfma_f32_16x16x128_f8f6f4 v[222:225], v[154:161], v[72:79], v[32:35]
	v_mfma_f32_16x16x128_f8f6f4 v[226:229], v[146:153], v[80:87], v[12:15]
	v_mfma_f32_16x16x128_f8f6f4 v[230:233], v[154:161], v[80:87], v[8:11]
	v_mfma_f32_16x16x128_f8f6f4 v[234:237], v[146:153], v[88:95], v[4:7]
	v_mfma_f32_16x16x128_f8f6f4 v[238:241], v[154:161], v[88:95], v[0:3]
	s_setprio 0
	s_barrier
	s_add_i32 s65, 0, 0x18000
	s_nop 2
	s_add_i32 s65, 0, 0x1c000
	ds_read_b128 v[0:3], v244 offset:32768
	ds_read_b128 v[8:11], v244 offset:34816
	ds_read_b128 v[4:7], v245 offset:32768
	ds_read_b128 v[12:15], v245 offset:34816
	ds_read_b128 v[128:131], v244 offset:49152
	ds_read_b128 v[138:141], v244 offset:51200
	ds_read_b128 v[132:135], v245 offset:49152
	ds_read_b128 v[142:145], v245 offset:51200
	s_mov_b32 m0, s33
	ds_read_b128 v[16:19], v250 offset:32768
	ds_read_b128 v[24:27], v250 offset:34816
	ds_read_b128 v[20:23], v251 offset:32768
	ds_read_b128 v[28:31], v251 offset:34816
	ds_read_b128 v[32:35], v250 offset:36864
	ds_read_b128 v[40:43], v250 offset:38912
	ds_read_b128 v[36:39], v251 offset:36864
	ds_read_b128 v[44:47], v251 offset:38912
	buffer_load_dwordx4 v248, s[8:11], s64 offen lds
	s_mov_b32 m0, s34
	s_nop 0
	buffer_load_dwordx4 v249, s[8:11], s64 offen lds
	s_waitcnt vmcnt(8)
	s_waitcnt lgkmcnt(0)
	s_barrier
	s_setprio 1
	s_waitcnt lgkmcnt(5)
	v_mfma_f32_16x16x128_f8f6f4 v[124:127], v[0:7], v[16:23], v[124:127]
	v_mfma_f32_16x16x128_f8f6f4 v[120:123], v[8:15], v[16:23], v[120:123]
	s_waitcnt lgkmcnt(4)
	v_mfma_f32_16x16x128_f8f6f4 v[116:119], v[0:7], v[24:31], v[116:119]
	v_mfma_f32_16x16x128_f8f6f4 v[112:115], v[8:15], v[24:31], v[112:115]
	s_waitcnt lgkmcnt(1)
	v_mfma_f32_16x16x128_f8f6f4 v[92:95], v[0:7], v[32:39], v[194:197]
	v_mfma_f32_16x16x128_f8f6f4 v[88:91], v[8:15], v[32:39], v[198:201]
	s_waitcnt lgkmcnt(0)
	v_mfma_f32_16x16x128_f8f6f4 v[84:87], v[0:7], v[40:47], v[202:205]
	v_mfma_f32_16x16x128_f8f6f4 v[80:83], v[8:15], v[40:47], v[206:209]
	s_setprio 0
	s_setprio 1
	v_mfma_f32_16x16x128_f8f6f4 v[108:111], v[128:135], v[16:23], v[108:111]
	v_mfma_f32_16x16x128_f8f6f4 v[104:107], v[138:145], v[16:23], v[104:107]
	v_mfma_f32_16x16x128_f8f6f4 v[100:103], v[128:135], v[24:31], v[100:103]
	v_mfma_f32_16x16x128_f8f6f4 v[96:99], v[138:145], v[24:31], v[96:99]
	v_mfma_f32_16x16x128_f8f6f4 v[76:79], v[128:135], v[32:39], v[162:165]
	v_mfma_f32_16x16x128_f8f6f4 v[72:75], v[138:145], v[32:39], v[166:169]
	v_mfma_f32_16x16x128_f8f6f4 v[68:71], v[128:135], v[40:47], v[170:173]
	v_mfma_f32_16x16x128_f8f6f4 v[64:67], v[138:145], v[40:47], v[174:177]
	s_setprio 0
	s_barrier
	s_mov_b32 m0, s36
	s_add_i32 s64, s62, 0x80
	ds_read_b128 v[32:35], v250 offset:49152
	ds_read_b128 v[146:149], v250 offset:51200
	ds_read_b128 v[36:39], v251 offset:49152
	ds_read_b128 v[150:153], v251 offset:51200
	ds_read_b128 v[154:157], v250 offset:53248
	ds_read_b128 v[162:165], v250 offset:55296
	ds_read_b128 v[158:161], v251 offset:53248
	ds_read_b128 v[166:169], v251 offset:55296
	buffer_load_dwordx4 v242, s[4:7], s64 offen lds
	s_mov_b32 m0, s37
	s_add_i32 s62, s62, 0x40080
	buffer_load_dwordx4 v243, s[4:7], s64 offen lds
	s_mov_b32 m0, s40
	s_nop 0
	buffer_load_dwordx4 v242, s[4:7], s62 offen lds
	s_mov_b32 m0, s41
	s_nop 0
	buffer_load_dwordx4 v243, s[4:7], s62 offen lds
	s_mov_b32 m0, s38
	s_nop 0
	buffer_load_dwordx4 v246, s[8:11], s63 offen lds
	s_mov_b32 m0, s39
	s_nop 0
	buffer_load_dwordx4 v247, s[8:11], s63 offen lds
	s_waitcnt vmcnt(8)
	s_waitcnt lgkmcnt(0)
	s_barrier
	s_setprio 1
	s_waitcnt lgkmcnt(5)
	v_mfma_f32_16x16x128_f8f6f4 v[60:63], v[0:7], v[32:39], v[60:63]
	v_mfma_f32_16x16x128_f8f6f4 v[56:59], v[8:15], v[32:39], v[56:59]
	s_waitcnt lgkmcnt(4)
	v_mfma_f32_16x16x128_f8f6f4 v[52:55], v[0:7], v[146:153], v[52:55]
	v_mfma_f32_16x16x128_f8f6f4 v[48:51], v[8:15], v[146:153], v[48:51]
	s_waitcnt lgkmcnt(1)
	v_mfma_f32_16x16x128_f8f6f4 v[28:31], v[0:7], v[154:161], v[178:181]
	v_mfma_f32_16x16x128_f8f6f4 v[24:27], v[8:15], v[154:161], v[182:185]
	s_waitcnt lgkmcnt(0)
	v_mfma_f32_16x16x128_f8f6f4 v[20:23], v[0:7], v[162:169], v[186:189]
	v_mfma_f32_16x16x128_f8f6f4 v[16:19], v[8:15], v[162:169], v[190:193]
	s_setprio 0
	s_setprio 1
	v_mfma_f32_16x16x128_f8f6f4 v[44:47], v[128:135], v[32:39], v[210:213]
	v_mfma_f32_16x16x128_f8f6f4 v[40:43], v[138:145], v[32:39], v[214:217]
	v_mfma_f32_16x16x128_f8f6f4 v[36:39], v[128:135], v[146:153], v[218:221]
	v_mfma_f32_16x16x128_f8f6f4 v[32:35], v[138:145], v[146:153], v[222:225]
	v_mfma_f32_16x16x128_f8f6f4 v[12:15], v[128:135], v[154:161], v[226:229]
	v_mfma_f32_16x16x128_f8f6f4 v[8:11], v[138:145], v[154:161], v[230:233]
	v_mfma_f32_16x16x128_f8f6f4 v[4:7], v[128:135], v[162:169], v[234:237]
	v_mfma_f32_16x16x128_f8f6f4 v[0:3], v[138:145], v[162:169], v[238:241]
	s_setprio 0
	s_barrier
	s_add_i32 s60, s60, 2
	s_addk_i32 s61, 0x100
	s_cmp_gt_u32 s60, 13
	s_cbranch_scc1 .LBB0_2279

.LBB0_2568:
	s_cmpk_lg_i32 s80, 0x180
	s_cbranch_scc1 .Lp11_fast
	v_add_u32_e32 v129, s36, v128
	v_ashrrev_i32_e32 v131, 3, v129
	v_lshlrev_b32_e32 v130, 4, v128
	v_lshlrev_b32_e32 v132, 1, v131
	v_lshrrev_b32_e32 v133, 2, v131
	v_bitop3_b32 v130, v129, s37, v130 bitop3:0x48
	v_and_b32_e32 v132, 24, v132
	v_and_b32_e32 v133, 4, v133
	v_and_b32_e32 v134, 0x1fffe3, v131
	v_lshl_add_u32 v129, v129, 4, v147
	v_or3_b32 v132, v134, v133, v132
	v_ashrrev_i32_e32 v129, 7, v129
	v_lshl_or_b32 v144, v132, 11, v130
	v_lshlrev_b32_e32 v132, 1, v129
	v_lshrrev_b32_e32 v133, 2, v129
	v_and_b32_e32 v132, 24, v132
	v_and_b32_e32 v133, 4, v133
	v_and_b32_e32 v134, 0x1fffe3, v129
	v_or3_b32 v132, v134, v133, v132
	v_lshrrev_b32_e32 v133, 3, v128
	v_lshl_or_b32 v145, v132, 11, v130
	v_and_b32_e32 v132, 15, v128
	v_and_b32_e32 v134, 0xffffffe, v133
	v_bfe_u32 v128, v128, 1, 3
	v_lshlrev_b32_e32 v132, 7, v132
	v_bitop3_b32 v133, v133, v128, s64 bitop3:0x6c
	v_bitop3_b32 v128, v134, v128, 1 bitop3:0x36
	v_or_b32_e32 v146, s58, v132
	v_or_b32_e32 v132, s59, v132
	v_lshlrev_b32_e32 v148, 4, v133
	v_lshlrev_b32_e32 v151, 4, v128
	v_add3_u32 v150, v148, v132, s65
	v_add3_u32 v152, v151, v132, s65
	v_lshl_or_b32 v250, v131, 11, v130
	v_lshl_or_b32 v251, v129, 11, v130
	v_add_u32_e32 v252, 0x40000, v250
	v_add_u32_e32 v253, 0x40000, v251
	v_add3_u32 v148, v148, v146, 0
	v_add3_u32 v146, v151, v146, 0
	s_branch .Lp11_join
.Lp11_fast:
.Lp11_join:
	ds_read_b128 v[128:131], v150 offset:0
	ds_read_b128 v[136:139], v150 offset:2048
	ds_read_b128 v[132:135], v152 offset:0
	ds_read_b128 v[140:143], v152 offset:2048
	ds_read_b128 v[154:157], v150 offset:16384
	ds_read_b128 v[162:165], v150 offset:18432
	ds_read_b128 v[158:161], v152 offset:16384
	ds_read_b128 v[166:169], v152 offset:18432
	s_add_i32 s6, s80, 0xffffff80
	s_add_i32 s7, s6, s75
	s_cmpk_eq_i32 s80, 0x880
	s_cselect_b32 s81, s71, s35
	s_cselect_b32 s11, 0x80, s80
	s_cselect_b32 s10, 0, s6
	s_cselect_b32 s6, s51, s7
	s_add_i32 s7, s81, s11
	s_add_i32 s11, s35, s80
	s_addk_i32 s11, 0xff00
	s_add_i32 s81, s81, s10
	s_mov_b32 m0, s60
	ds_read_b128 v[170:173], v148
	ds_read_b128 v[178:181], v148 offset:2048
	ds_read_b128 v[174:177], v146
	ds_read_b128 v[182:185], v146 offset:2048
	ds_read_b128 v[186:189], v148 offset:4096
	ds_read_b128 v[194:197], v148 offset:6144
	ds_read_b128 v[190:193], v146 offset:4096
	ds_read_b128 v[198:201], v146 offset:6144
	buffer_load_dwordx4 v252, s[88:91], s11 offen lds
	s_mov_b32 m0, s63
	s_nop 0
	buffer_load_dwordx4 v253, s[88:91], s11 offen lds
	s_waitcnt vmcnt(8)
	s_waitcnt lgkmcnt(0)
	s_barrier
	s_setprio 1
	s_waitcnt lgkmcnt(0)
	v_mfma_f32_16x16x128_f8f6f4 v[124:127], v[128:135], v[170:177], v[124:127]
	v_mfma_f32_16x16x128_f8f6f4 v[120:123], v[136:143], v[170:177], v[120:123]
	v_mfma_f32_16x16x128_f8f6f4 v[116:119], v[128:135], v[178:185], v[116:119]
	v_mfma_f32_16x16x128_f8f6f4 v[112:115], v[136:143], v[178:185], v[112:115]
	v_mfma_f32_16x16x128_f8f6f4 v[96:99], v[128:135], v[186:193], v[96:99]
	v_mfma_f32_16x16x128_f8f6f4 v[202:205], v[136:143], v[186:193], v[88:91]
	v_mfma_f32_16x16x128_f8f6f4 v[206:209], v[128:135], v[194:201], v[80:83]
	v_mfma_f32_16x16x128_f8f6f4 v[210:213], v[136:143], v[194:201], v[72:75]
	s_setprio 0
	s_setprio 1
	v_mfma_f32_16x16x128_f8f6f4 v[108:111], v[154:161], v[170:177], v[108:111]
	v_mfma_f32_16x16x128_f8f6f4 v[104:107], v[162:169], v[170:177], v[104:107]
	v_mfma_f32_16x16x128_f8f6f4 v[100:103], v[154:161], v[178:185], v[100:103]
	v_mfma_f32_16x16x128_f8f6f4 v[170:173], v[162:169], v[178:185], v[92:95]
	v_mfma_f32_16x16x128_f8f6f4 v[174:177], v[154:161], v[186:193], v[84:87]
	v_mfma_f32_16x16x128_f8f6f4 v[178:181], v[162:169], v[186:193], v[76:79]
	v_mfma_f32_16x16x128_f8f6f4 v[182:185], v[154:161], v[194:201], v[68:71]
	v_mfma_f32_16x16x128_f8f6f4 v[186:189], v[162:169], v[194:201], v[64:67]
	s_setprio 0
	s_barrier
	s_mov_b32 m0, s43
	s_mov_b32 s10, s90
	s_mov_b32 s11, s91
	s_nop 1
	ds_read_b128 v[64:67], v148 offset:16384
	ds_read_b128 v[72:75], v148 offset:18432
	ds_read_b128 v[68:71], v146 offset:16384
	ds_read_b128 v[76:79], v146 offset:18432
	ds_read_b128 v[80:83], v148 offset:20480
	ds_read_b128 v[88:91], v148 offset:22528
	ds_read_b128 v[84:87], v146 offset:20480
	ds_read_b128 v[92:95], v146 offset:22528
	buffer_load_dwordx4 v144, s[8:11], s6 offen lds
	s_mov_b32 m0, s44
	s_add_i32 s82, s6, 0x40000
	buffer_load_dwordx4 v145, s[8:11], s6 offen lds
	s_mov_b32 m0, s45
	s_nop 0
	buffer_load_dwordx4 v144, s[8:11], s82 offen lds
	s_mov_b32 m0, s46
	s_nop 0
	buffer_load_dwordx4 v145, s[8:11], s82 offen lds
	s_mov_b32 m0, s42
	s_nop 0
	buffer_load_dwordx4 v250, s[88:91], s81 offen lds
	s_mov_b32 m0, s47
	s_nop 0
	buffer_load_dwordx4 v251, s[88:91], s81 offen lds
	s_waitcnt vmcnt(8)
	s_waitcnt lgkmcnt(0)
	s_barrier
	s_setprio 1
	s_waitcnt lgkmcnt(5)
	v_mfma_f32_16x16x128_f8f6f4 v[60:63], v[128:135], v[64:71], v[60:63]
	v_mfma_f32_16x16x128_f8f6f4 v[56:59], v[136:143], v[64:71], v[56:59]
	s_waitcnt lgkmcnt(4)
	v_mfma_f32_16x16x128_f8f6f4 v[48:51], v[128:135], v[72:79], v[48:51]
	v_mfma_f32_16x16x128_f8f6f4 v[190:193], v[136:143], v[72:79], v[40:43]
	s_waitcnt lgkmcnt(1)
	v_mfma_f32_16x16x128_f8f6f4 v[194:197], v[128:135], v[80:87], v[32:35]
	v_mfma_f32_16x16x128_f8f6f4 v[198:201], v[136:143], v[80:87], v[24:27]
	s_waitcnt lgkmcnt(0)
	v_mfma_f32_16x16x128_f8f6f4 v[214:217], v[128:135], v[88:95], v[16:19]
	v_mfma_f32_16x16x128_f8f6f4 v[218:221], v[136:143], v[88:95], v[8:11]
	s_setprio 0
	s_setprio 1
	v_mfma_f32_16x16x128_f8f6f4 v[52:55], v[154:161], v[64:71], v[52:55]
	v_mfma_f32_16x16x128_f8f6f4 v[222:225], v[162:169], v[64:71], v[44:47]
	v_mfma_f32_16x16x128_f8f6f4 v[226:229], v[154:161], v[72:79], v[36:39]
	v_mfma_f32_16x16x128_f8f6f4 v[230:233], v[162:169], v[72:79], v[28:31]
	v_mfma_f32_16x16x128_f8f6f4 v[234:237], v[154:161], v[80:87], v[20:23]
	v_mfma_f32_16x16x128_f8f6f4 v[238:241], v[162:169], v[80:87], v[12:15]
	v_mfma_f32_16x16x128_f8f6f4 v[242:245], v[154:161], v[88:95], v[4:7]
	v_mfma_f32_16x16x128_f8f6f4 v[246:249], v[162:169], v[88:95], v[0:3]
	s_setprio 0
	s_barrier
	s_add_i32 s82, 0, 0x18000
	s_nop 2
	s_add_i32 s82, 0, 0x1c000
	ds_read_b128 v[0:3], v150 offset:32768
	ds_read_b128 v[8:11], v150 offset:34816
	ds_read_b128 v[4:7], v152 offset:32768
	ds_read_b128 v[12:15], v152 offset:34816
	ds_read_b128 v[128:131], v150 offset:49152
	ds_read_b128 v[136:139], v150 offset:51200
	ds_read_b128 v[132:135], v152 offset:49152
	ds_read_b128 v[140:143], v152 offset:51200
	s_mov_b32 m0, s48
	ds_read_b128 v[16:19], v148 offset:32768
	ds_read_b128 v[24:27], v148 offset:34816
	ds_read_b128 v[20:23], v146 offset:32768
	ds_read_b128 v[28:31], v146 offset:34816
	ds_read_b128 v[32:35], v148 offset:36864
	ds_read_b128 v[40:43], v148 offset:38912
	ds_read_b128 v[36:39], v146 offset:36864
	ds_read_b128 v[44:47], v146 offset:38912
	buffer_load_dwordx4 v252, s[88:91], s81 offen lds
	s_mov_b32 m0, s49
	s_nop 0
	buffer_load_dwordx4 v253, s[88:91], s81 offen lds
	s_waitcnt vmcnt(8)
	s_waitcnt lgkmcnt(0)
	s_barrier
	s_setprio 1
	s_waitcnt lgkmcnt(5)
	v_mfma_f32_16x16x128_f8f6f4 v[124:127], v[0:7], v[16:23], v[124:127]
	v_mfma_f32_16x16x128_f8f6f4 v[120:123], v[8:15], v[16:23], v[120:123]
	s_waitcnt lgkmcnt(4)
	v_mfma_f32_16x16x128_f8f6f4 v[116:119], v[0:7], v[24:31], v[116:119]
	v_mfma_f32_16x16x128_f8f6f4 v[112:115], v[8:15], v[24:31], v[112:115]
	s_waitcnt lgkmcnt(1)
	v_mfma_f32_16x16x128_f8f6f4 v[96:99], v[0:7], v[32:39], v[96:99]
	v_mfma_f32_16x16x128_f8f6f4 v[88:91], v[8:15], v[32:39], v[202:205]
	s_waitcnt lgkmcnt(0)
	v_mfma_f32_16x16x128_f8f6f4 v[80:83], v[0:7], v[40:47], v[206:209]
	v_mfma_f32_16x16x128_f8f6f4 v[72:75], v[8:15], v[40:47], v[210:213]
	s_setprio 0
	s_setprio 1
	v_mfma_f32_16x16x128_f8f6f4 v[108:111], v[128:135], v[16:23], v[108:111]
	v_mfma_f32_16x16x128_f8f6f4 v[104:107], v[136:143], v[16:23], v[104:107]
	v_mfma_f32_16x16x128_f8f6f4 v[100:103], v[128:135], v[24:31], v[100:103]
	v_mfma_f32_16x16x128_f8f6f4 v[92:95], v[136:143], v[24:31], v[170:173]
	v_mfma_f32_16x16x128_f8f6f4 v[84:87], v[128:135], v[32:39], v[174:177]
	v_mfma_f32_16x16x128_f8f6f4 v[76:79], v[136:143], v[32:39], v[178:181]
	v_mfma_f32_16x16x128_f8f6f4 v[68:71], v[128:135], v[40:47], v[182:185]
	v_mfma_f32_16x16x128_f8f6f4 v[64:67], v[136:143], v[40:47], v[186:189]
	s_setprio 0
	s_barrier
	s_mov_b32 m0, s52
	s_add_i32 s81, s6, 0x80
	ds_read_b128 v[154:157], v148 offset:49152
	ds_read_b128 v[162:165], v148 offset:51200
	ds_read_b128 v[158:161], v146 offset:49152
	ds_read_b128 v[166:169], v146 offset:51200
	ds_read_b128 v[170:173], v148 offset:53248
	ds_read_b128 v[178:181], v148 offset:55296
	ds_read_b128 v[174:177], v146 offset:53248
	ds_read_b128 v[182:185], v146 offset:55296
	buffer_load_dwordx4 v144, s[8:11], s81 offen lds
	s_mov_b32 m0, s53
	s_add_i32 s6, s6, 0x40080
	buffer_load_dwordx4 v145, s[8:11], s81 offen lds
	s_mov_b32 m0, s56
	s_nop 0
	buffer_load_dwordx4 v144, s[8:11], s6 offen lds
	s_mov_b32 m0, s57
	s_nop 0
	buffer_load_dwordx4 v145, s[8:11], s6 offen lds
	s_mov_b32 m0, s54
	s_nop 0
	buffer_load_dwordx4 v250, s[88:91], s7 offen lds
	s_mov_b32 m0, s55
	s_nop 0
	buffer_load_dwordx4 v251, s[88:91], s7 offen lds
	s_waitcnt vmcnt(8)
	s_waitcnt lgkmcnt(0)
	s_barrier
	s_setprio 1
	s_waitcnt lgkmcnt(5)
	v_mfma_f32_16x16x128_f8f6f4 v[60:63], v[0:7], v[154:161], v[60:63]
	v_mfma_f32_16x16x128_f8f6f4 v[56:59], v[8:15], v[154:161], v[56:59]
	s_waitcnt lgkmcnt(4)
	v_mfma_f32_16x16x128_f8f6f4 v[48:51], v[0:7], v[162:169], v[48:51]
	v_mfma_f32_16x16x128_f8f6f4 v[40:43], v[8:15], v[162:169], v[190:193]
	s_waitcnt lgkmcnt(1)
	v_mfma_f32_16x16x128_f8f6f4 v[32:35], v[0:7], v[170:177], v[194:197]
	v_mfma_f32_16x16x128_f8f6f4 v[24:27], v[8:15], v[170:177], v[198:201]
	s_waitcnt lgkmcnt(0)
	v_mfma_f32_16x16x128_f8f6f4 v[16:19], v[0:7], v[178:185], v[214:217]
	v_mfma_f32_16x16x128_f8f6f4 v[8:11], v[8:15], v[178:185], v[218:221]
	s_setprio 0
	s_setprio 1
	v_mfma_f32_16x16x128_f8f6f4 v[52:55], v[128:135], v[154:161], v[52:55]
	v_mfma_f32_16x16x128_f8f6f4 v[44:47], v[136:143], v[154:161], v[222:225]
	v_mfma_f32_16x16x128_f8f6f4 v[36:39], v[128:135], v[162:169], v[226:229]
	v_mfma_f32_16x16x128_f8f6f4 v[28:31], v[136:143], v[162:169], v[230:233]
	v_mfma_f32_16x16x128_f8f6f4 v[20:23], v[128:135], v[170:177], v[234:237]
	v_mfma_f32_16x16x128_f8f6f4 v[12:15], v[136:143], v[170:177], v[238:241]
	v_mfma_f32_16x16x128_f8f6f4 v[4:7], v[128:135], v[178:185], v[242:245]
	v_mfma_f32_16x16x128_f8f6f4 v[0:3], v[136:143], v[178:185], v[246:249]
	s_setprio 0
	s_barrier
	s_add_i32 s79, s79, 2
	s_addk_i32 s80, 0x100
	s_cmp_gt_u32 s79, 13
	s_cbranch_scc1 .LBB0_2574
